# gate/up and down item setup: row-list / row-weight loads issued together (2 and 4 serial load+wait steps became 1 and 2)
# speedup vs baseline: 1.0350x; 1.0038x over previous
.LBB0_1300:
	s_or_b64 exec, exec, s[0:1]
	v_mov_b32_e32 v2, v231
	s_nop 0
	v_add_u32_e32 v218, s48, v2
	v_add_u32_e32 v218, 0x200, v218
	v_cmp_gt_i32_e32 vcc, s84, v218
	s_and_saveexec_b64 s[0:1], vcc
	s_cbranch_execz .LBB0_1302
	v_mov_b32_e32 v218, v2
	v_ashrrev_i32_e32 v219, 31, v2
	s_ashr_i32 s49, s48, 31
	v_lshl_add_u64 v[218:219], v[218:219], 0, s[48:49]
	v_lshl_add_u64 v[218:219], v[218:219], 2, s[70:71]
	global_load_dword v0, v[218:219], off offset:2048
.LBB0_1302:
	s_or_b64 exec, exec, s[0:1]
	s_add_i32 s0, s29, 0xfffffdbf
	v_lshl_add_u32 v2, v2, 2, 0
	v_mov_b32_e32 v235, v231
	s_cmp_lt_u32 s0, 0xffffffc0
	s_waitcnt vmcnt(0)
	ds_write_b32 v2, v3 offset:55296
	ds_write_b32 v2, v0 offset:57344
	s_waitcnt lgkmcnt(0)
	s_barrier
	s_cselect_b64 s[0:1], -1, 0
	v_and_b32_e32 v234, 31, v235
	s_or_b64 s[42:43], s[68:69], s[0:1]
	v_and_b32_e32 v233, 32, v235
	v_and_b32_e32 v0, 7, v235
	v_mul_u32_u24_e32 v2, 0x48, v234
	s_mov_b64 s[0:1], -1
	s_and_b64 vcc, exec, s[42:43]
	v_lshlrev_b32_e32 v237, 4, v0
	v_or_b32_e32 v236, s28, v0
	v_add_lshl_u32 v232, v2, v233, 1
	s_cbranch_vccnz .LBB0_1320
	v_lshrrev_b32_e32 v0, 2, v235
	v_readlane_b32 s0, v255, 5
	v_mov_b32_e32 v240, v232
	v_readlane_b32 s1, v255, 9
	v_and_or_b32 v0, v0, 14, s0
	s_movk_i32 s0, 0x48
	v_mul_lo_u32 v2, v236, s0
	v_lshl_or_b32 v238, v0, 10, v237
	v_add_lshl_u32 v239, v2, v0, 1
	v_lshlrev_b32_e32 v0, 2, v234
	v_readlane_b32 s0, v255, 7
	s_mov_b64 s[42:43], s[36:37]
	v_add_u32_e32 v244, 0, v239
	v_add_u32_e32 v2, s0, v0
	v_add_u32_e32 v2, 0xd800, v2
	ds_read2_b32 v[2:3], v2 offset1:32
	s_mov_b32 s0, 0x24000
	v_add_u32_e32 v0, s1, v0
	s_cmp_lt_i32 s83, s29
	v_add_u32_e32 v245, 0, v240
	s_waitcnt lgkmcnt(0)
	v_lshlrev_b32_e32 v4, 7, v2
	v_and_b32_e32 v4, 0xfffffc00, v4
	v_cmp_ne_u32_e32 vcc, s0, v2
	s_mov_b32 s2, 0
	v_add_u32_e32 v246, s33, v245
	v_cndmask_b32_e32 v2, 0, v4, vcc
	v_or_b32_e32 v241, v2, v233
	v_lshlrev_b32_e32 v2, 7, v3
	v_and_b32_e32 v2, 0xfffffc00, v2
	v_cmp_ne_u32_e32 vcc, s0, v3
	s_movk_i32 s49, 0x80
	s_mov_b32 s39, 0
	v_cndmask_b32_e32 v2, 0, v2, vcc
	v_or_b32_e32 v242, v2, v233
	global_load_dwordx4 v[204:207], v241, s[54:55] offset:16
	global_load_dwordx4 v[212:215], v241, s[54:55]
	global_load_dwordx4 v[192:195], v242, s[54:55] offset:16
	global_load_dwordx4 v[208:211], v242, s[54:55]
	ds_read_b32 v0, v0 offset:57344
	s_waitcnt lgkmcnt(0)
	v_lshlrev_b32_e32 v2, 7, v0
	v_and_b32_e32 v2, 0xfffffc00, v2
	v_cmp_ne_u32_e32 vcc, s0, v0
	s_mov_b64 s[0:1], s[34:35]
	s_nop 0
	v_cndmask_b32_e32 v0, 0, v2, vcc
	v_or_b32_e32 v243, v0, v233
	v_mov_b32_e32 v0, v238
	global_load_dwordx4 v[200:203], v243, s[54:55] offset:16
	global_load_dwordx4 v[196:199], v243, s[54:55]
	global_load_dwordx4 v[2:5], v0, s[0:1] nt
	global_load_dwordx4 v[6:9], v0, s[0:1] offset:1024 nt
	global_load_dwordx4 v[10:13], v0, s[42:43] nt
	global_load_dwordx4 v[14:17], v0, s[42:43] offset:1024 nt
	s_mov_b64 s[0:1], s[92:93]
	s_mov_b64 s[42:43], s[96:97]
	v_mov_b32_e32 v0, v238
	global_load_dwordx4 v[160:163], v0, s[42:43] nt
	global_load_dwordx4 v[164:167], v0, s[42:43] offset:1024 nt
	global_load_dwordx4 v[168:171], v0, s[0:1] nt
	global_load_dwordx4 v[172:175], v0, s[0:1] offset:1024 nt
	s_mov_b64 s[42:43], s[88:89]
	s_mov_b64 s[0:1], s[8:9]
	s_waitcnt vmcnt(6)
	v_cvt_pk_bf16_f32 v0, v2, v6
	v_mov_b32_e32 v6, v1
	s_waitcnt vmcnt(4)
	v_cvt_pk_bf16_f32 v2, v10, v14
	ds_write2_b32 v244, v0, v2 offset1:8
	v_cvt_pk_bf16_f32 v0, v3, v7
	v_cvt_pk_bf16_f32 v2, v11, v15
	v_add_u32_e32 v3, 0x400, v244
	ds_write2_b32 v3, v0, v2 offset0:32 offset1:40
	v_cvt_pk_bf16_f32 v0, v4, v8
	v_cvt_pk_bf16_f32 v2, v12, v16
	v_add_u32_e32 v3, 0x800, v244
	ds_write2_b32 v3, v0, v2 offset0:64 offset1:72
	v_cvt_pk_bf16_f32 v0, v5, v9
	v_cvt_pk_bf16_f32 v2, v13, v17
	v_add_u32_e32 v3, 0xc00, v244
	ds_write2_b32 v3, v0, v2 offset0:96 offset1:104
	v_mov_b32_e32 v0, v238
	global_load_dwordx4 v[176:179], v0, s[42:43] nt
	global_load_dwordx4 v[180:183], v0, s[42:43] offset:1024 nt
	global_load_dwordx4 v[184:187], v0, s[0:1] nt
	global_load_dwordx4 v[188:191], v0, s[0:1] offset:1024 nt
	v_mov_b32_e32 v14, v1
	v_mov_b32_e32 v15, v1
	s_cselect_b64 s[0:1], -1, 0
	v_mov_b32_e32 v0, v1
	v_mov_b32_e32 v2, v1
	v_mov_b32_e32 v3, v1
	v_mov_b32_e32 v4, v1
	v_mov_b32_e32 v5, v1
	v_mov_b32_e32 v7, v1
	v_mov_b32_e32 v8, v1
	v_mov_b32_e32 v9, v1
	v_mov_b32_e32 v10, v1
	v_mov_b32_e32 v11, v1
	v_mov_b32_e32 v12, v1
	v_mov_b32_e32 v13, v1
	v_mov_b32_e32 v16, 0
	s_cmp_lt_i32 s80, s29
	v_mov_b64_e32 v[46:47], v[14:15]
	v_mov_b64_e32 v[78:79], v[14:15]
	v_mov_b64_e32 v[62:63], v[14:15]
	v_mov_b64_e32 v[94:95], v[14:15]
	v_mov_b64_e32 v[110:111], v[14:15]
	v_mov_b64_e32 v[142:143], v[14:15]
	v_mov_b64_e32 v[126:127], v[14:15]
	v_mov_b64_e32 v[158:159], v[14:15]
	s_cselect_b64 s[44:45], -1, 0
	v_mov_b64_e32 v[44:45], v[12:13]
	v_mov_b64_e32 v[42:43], v[10:11]
	v_mov_b64_e32 v[40:41], v[8:9]
	v_mov_b64_e32 v[38:39], v[6:7]
	v_mov_b64_e32 v[36:37], v[4:5]
	v_mov_b64_e32 v[34:35], v[2:3]
	v_mov_b64_e32 v[32:33], v[0:1]
	v_mov_b64_e32 v[76:77], v[12:13]
	v_mov_b64_e32 v[74:75], v[10:11]
	v_mov_b64_e32 v[72:73], v[8:9]
	v_mov_b64_e32 v[70:71], v[6:7]
	v_mov_b64_e32 v[68:69], v[4:5]
	v_mov_b64_e32 v[66:67], v[2:3]
	v_mov_b64_e32 v[64:65], v[0:1]
	v_mov_b64_e32 v[60:61], v[12:13]
	v_mov_b64_e32 v[58:59], v[10:11]
	v_mov_b64_e32 v[56:57], v[8:9]
	v_mov_b64_e32 v[54:55], v[6:7]
	v_mov_b64_e32 v[52:53], v[4:5]
	v_mov_b64_e32 v[50:51], v[2:3]
	v_mov_b64_e32 v[48:49], v[0:1]
	v_mov_b64_e32 v[92:93], v[12:13]
	v_mov_b64_e32 v[90:91], v[10:11]
	v_mov_b64_e32 v[88:89], v[8:9]
	v_mov_b64_e32 v[86:87], v[6:7]
	v_mov_b64_e32 v[84:85], v[4:5]
	v_mov_b64_e32 v[82:83], v[2:3]
	v_mov_b64_e32 v[80:81], v[0:1]
	v_mov_b64_e32 v[108:109], v[12:13]
	v_mov_b64_e32 v[106:107], v[10:11]
	v_mov_b64_e32 v[104:105], v[8:9]
	v_mov_b64_e32 v[102:103], v[6:7]
	v_mov_b64_e32 v[100:101], v[4:5]
	v_mov_b64_e32 v[98:99], v[2:3]
	v_mov_b64_e32 v[96:97], v[0:1]
	v_mov_b64_e32 v[140:141], v[12:13]
	v_mov_b64_e32 v[138:139], v[10:11]
	v_mov_b64_e32 v[136:137], v[8:9]
	v_mov_b64_e32 v[134:135], v[6:7]
	v_mov_b64_e32 v[132:133], v[4:5]
	v_mov_b64_e32 v[130:131], v[2:3]
	v_mov_b64_e32 v[128:129], v[0:1]
	v_mov_b64_e32 v[124:125], v[12:13]
	v_mov_b64_e32 v[122:123], v[10:11]
	v_mov_b64_e32 v[120:121], v[8:9]
	v_mov_b64_e32 v[118:119], v[6:7]
	v_mov_b64_e32 v[116:117], v[4:5]
	v_mov_b64_e32 v[114:115], v[2:3]
	v_mov_b64_e32 v[112:113], v[0:1]
	v_mov_b64_e32 v[156:157], v[12:13]
	v_mov_b64_e32 v[154:155], v[10:11]
	v_mov_b64_e32 v[152:153], v[8:9]
	v_mov_b64_e32 v[150:151], v[6:7]
	v_mov_b64_e32 v[148:149], v[4:5]
	v_mov_b64_e32 v[146:147], v[2:3]
	v_mov_b64_e32 v[144:145], v[0:1]
	v_mov_b32_e32 v17, v16
	v_mov_b32_e32 v18, v16
	v_mov_b32_e32 v19, v16
	v_mov_b32_e32 v20, v16
	v_mov_b32_e32 v21, v16
	v_mov_b32_e32 v22, v16
	v_mov_b32_e32 v23, v16
	v_mov_b32_e32 v24, v16
	v_mov_b32_e32 v25, v16
	v_mov_b32_e32 v26, v16
	v_mov_b32_e32 v27, v16
	v_mov_b32_e32 v28, v16
	v_mov_b32_e32 v29, v16
	v_mov_b32_e32 v30, v16
	v_mov_b32_e32 v31, v16
	s_branch .LBB0_1306

.LBB0_1419:
	s_sub_i32 s56, s76, s44
	s_cmpk_lt_i32 s56, 0x241
	s_cselect_b64 s[42:43], -1, 0
	s_and_b64 s[62:63], s[36:37], s[42:43]
	s_mov_b64 s[42:43], -1
	s_and_b64 vcc, exec, s[62:63]
	s_cbranch_vccnz .LBB0_1418
	v_mov_b32_e32 v0, v231
	v_mov_b32_e32 v2, 0x24000
	v_mov_b32_e32 v218, 0x24000
	v_add_u32_e32 v4, s44, v0
	v_cmp_gt_i32_e32 vcc, s76, v4
	s_and_saveexec_b64 s[42:43], vcc
	s_cbranch_execz .Ldf_a
	v_ashrrev_i32_e32 v5, 31, v4
	v_lshl_add_u64 v[4:5], v[4:5], 2, s[46:47]
	global_load_dword v2, v[4:5], off
.Ldf_a:
	s_or_b64 exec, exec, s[42:43]
	v_add_u32_e32 v4, s44, v0
	v_add_u32_e32 v4, 0x200, v4
	v_cmp_gt_i32_e32 vcc, s76, v4
	s_and_saveexec_b64 s[42:43], vcc
	s_cbranch_execz .Ldf_b
	v_mov_b32_e32 v4, v0
	v_ashrrev_i32_e32 v5, 31, v0
	s_ashr_i32 s45, s44, 31
	v_lshl_add_u64 v[4:5], v[4:5], 0, s[44:45]
	v_lshl_add_u64 v[4:5], v[4:5], 2, s[46:47]
	global_load_dword v218, v[4:5], off offset:2048
.Ldf_b:
	s_or_b64 exec, exec, s[42:43]
	s_mov_b32 s25, 0x20000
	v_lshl_add_u32 v0, v0, 2, 0
	v_mov_b32_e32 v3, 0
	v_mov_b32_e32 v219, 0
	s_waitcnt vmcnt(0)
	ds_write_b32 v0, v2 offset:55296
	ds_write_b32 v0, v218 offset:57344
	v_cmp_gt_i32_e32 vcc, s25, v2
	s_and_saveexec_b64 s[42:43], vcc
	s_cbranch_execz .Ldf_c
	v_mov_b32_e32 v4, v2
	v_ashrrev_i32_e32 v5, 31, v2
	v_lshl_add_u64 v[4:5], v[4:5], 2, s[18:19]
	global_load_dword v3, v[4:5], off
.Ldf_c:
	s_or_b64 exec, exec, s[42:43]
	v_cmp_gt_i32_e32 vcc, s25, v218
	s_and_saveexec_b64 s[42:43], vcc
	s_cbranch_execz .Ldf_d
	v_mov_b32_e32 v4, v218
	v_ashrrev_i32_e32 v5, 31, v218
	v_lshl_add_u64 v[4:5], v[4:5], 2, s[18:19]
	global_load_dword v219, v[4:5], off
.Ldf_d:
	s_or_b64 exec, exec, s[42:43]
	v_mov_b32_e32 v4, v231
	s_waitcnt vmcnt(0)
	v_mul_f32_e32 v3, 0x41800000, v3
	v_mul_f32_e32 v219, 0x41800000, v219
	ds_write_b32 v0, v3 offset:59392
	s_mov_b64 s[42:43], 0
.LBB0_1428:
	s_or_b64 exec, exec, s[42:43]
	v_mov_b32_e32 v239, v233
	v_mov_b32_e32 v240, v234
	v_mov_b32_e32 v241, v235
	ds_write_b32 v0, v219 offset:61440
	s_waitcnt lgkmcnt(0)
	s_barrier
	ds_read2_b32 v[2:3], v238 offset1:32
	s_add_i32 s25, s56, 0xfffffdbf
	s_cmp_gt_u32 s25, 0xffffffbf
	s_cselect_b64 s[42:43], -1, 0
	s_xor_b64 s[62:63], s[36:37], -1
	s_waitcnt lgkmcnt(0)
	v_lshl_or_b32 v242, v2, 8, v232
	v_lshl_or_b32 v243, v3, 8, v232
	global_load_dwordx4 v[204:207], v242, s[30:31] offset:16
	global_load_dwordx4 v[212:215], v242, s[30:31]
	global_load_dwordx4 v[192:195], v243, s[30:31] offset:16
	global_load_dwordx4 v[208:211], v243, s[30:31]
	s_and_b64 s[62:63], s[62:63], s[42:43]
	v_mov_b32_e32 v0, 0x2400000
	s_and_b64 vcc, exec, s[62:63]
	s_cbranch_vccz .LBB0_1430
	ds_read_b32 v0, v237 offset:57344
	s_waitcnt lgkmcnt(0)
	v_lshlrev_b32_e32 v0, 8, v0
